# k_csr_fallback: wave-uniform overflow-flag check via scalar s_load_dword + s_cmp instead of vector global_load sc1 + v_cmp
# speedup vs baseline: 1.0012x; 1.0012x over previous
_Z14k_csr_fallbackPKiS0_S0_PKfS2_S2_S2_S2_PDv8_DF16_S4_S4_S4_PiS5_PfS4_S2_PDF16_:
	s_load_dwordx2 s[2:3], s[0:1], 0x0
	v_mov_b32_e32 v2, 0
	s_waitcnt lgkmcnt(0)
	s_load_dword s4, s[2:3], 0x0
	s_waitcnt lgkmcnt(0)
	s_cmp_eq_u32 s4, 0
	s_cbranch_scc1 .LBB0_107
	s_load_dwordx2 s[28:29], s[0:1], 0x88
	s_load_dwordx8 s[4:11], s[0:1], 0x68
	s_load_dwordx8 s[12:19], s[0:1], 0x48
	s_load_dwordx8 s[36:43], s[0:1], 0x28
	s_load_dwordx8 s[20:27], s[0:1], 0x8
	v_or_b32_e32 v1, 0xfffffc00, v0
	v_lshlrev_b32_e32 v3, 2, v0
	s_mov_b64 s[0:1], 0
	s_movk_i32 s2, 0x4a1f
	v_mov_b32_e32 v4, v1
